# peersel middle stage variant: 2 lanes per row with 64 keys each on two waves per half (other half on the other two SIMDs): four sort16, three local merges, one cross-lane merge
# baseline (speedup 1.0000x reference)
; #define MFMA16(a, b, c) __builtin_amdgcn_mfma_f32_16x16x32_bf16((a), (b), (c), 0, 0, 0)
; DI void peer_select_unit(const Params& p, int unit, char* lds, const bf16x8 (&kb)[4][4]) {
;     ...
;   {
;     const int set = wid >> 1, kh = wid & 1;
;     bf16x8 qa[2][4];
; #pragma unroll
;     for (int mt = 0; mt < 2; ++mt)
; #pragma unroll
;       for (int kk = 0; kk < 4; ++kk) qa[mt][kk] = *(const bf16x8*)(qy + (size_t)(t0 + 16 * mt + fr) * 2048 + h * 256 + set * 128 + kk * 32 + fq * 8);
; #pragma unroll
;     for (int mt = 0; mt < 2; ++mt)
; #pragma unroll
;       for (int nj = 0; nj < 4; ++nj) {
;         f32x4 d = {0.f, 0.f, 0.f, 0.f};
; #pragma unroll
;         for (int kk = 0; kk < 4; ++kk) d = MFMA16(qa[mt][kk], kb[nj][kk], d);
; #pragma unroll
;         for (int r = 0; r < 4; ++r) sc[(set * 32 + 16 * mt + 4 * fq + r) * 132 + 64 * kh + 16 * nj + fr] = d[r];
;       }
;   }
.LBB0_1652:
	v_lshlrev_b32_e32 v64, 2, v72
	v_mov_b32_e32 v66, v206
	v_and_b32_e32 v73, 7, v72
	v_and_b32_e32 v74, 0xffffffe0, v64
	v_lshlrev_b32_e32 v64, 9, v73
	v_and_or_b32 v84, v66, 15, v74
	v_and_b32_e32 v70, 0xffffff80, v66
	v_bfe_u32 v67, v66, 4, 2
	v_lshl_add_u64 v[68:69], s[58:59], 0, v[64:65]
	v_ashrrev_i32_e32 v71, 31, v70
	v_or_b32_e32 v90, 16, v84
	v_lshl_add_u64 v[68:69], v[70:71], 1, v[68:69]
	v_lshlrev_b32_e32 v64, 4, v67
	v_ashrrev_i32_e32 v85, 31, v84
	v_ashrrev_i32_e32 v91, 31, v90
	v_lshl_add_u64 v[88:89], v[68:69], 0, v[64:65]
	v_lshlrev_b64 v[68:69], 12, v[84:85]
	v_lshlrev_b64 v[90:91], 12, v[90:91]
	v_lshl_add_u64 v[116:117], v[88:89], 0, v[68:69]
	v_lshl_add_u64 v[120:121], v[88:89], 0, v[90:91]
	s_barrier
	s_waitcnt vmcnt(0)
	v_mov_b32_e32 v68, v148
	v_mov_b32_e32 v69, v149
	v_mov_b32_e32 v70, v150
	v_mov_b32_e32 v71, v151
	v_mov_b32_e32 v76, v152
	v_mov_b32_e32 v77, v153
	v_mov_b32_e32 v78, v154
	v_mov_b32_e32 v79, v155
	v_mov_b32_e32 v92, v156
	v_mov_b32_e32 v93, v157
	v_mov_b32_e32 v94, v158
	v_mov_b32_e32 v95, v159
	v_mov_b32_e32 v96, v160
	v_mov_b32_e32 v97, v161
	v_mov_b32_e32 v98, v162
	v_mov_b32_e32 v99, v163
	v_ashrrev_i32_e32 v75, 2, v66
	v_and_b32_e32 v64, 0x4f, v66
	v_lshlrev_b32_e32 v64, 2, v64
	s_mov_b64 s[20:21], -1
	s_mov_b32 s69, 0
	v_mfma_f32_16x16x32_bf16 v[80:83], v[68:71], v[0:3], 0
	v_mfma_f32_16x16x32_bf16 v[84:87], v[68:71], v[56:59], 0
	v_mfma_f32_16x16x32_bf16 v[88:91], v[68:71], v[24:27], 0
	v_mfma_f32_16x16x32_bf16 v[68:71], v[68:71], v[44:47], 0
	v_mfma_f32_16x16x32_bf16 v[100:103], v[92:95], v[0:3], 0
	v_mfma_f32_16x16x32_bf16 v[104:107], v[92:95], v[56:59], 0
	v_mfma_f32_16x16x32_bf16 v[108:111], v[92:95], v[24:27], 0
	v_mfma_f32_16x16x32_bf16 v[80:83], v[76:79], v[4:7], v[80:83]
	v_mfma_f32_16x16x32_bf16 v[84:87], v[76:79], v[16:19], v[84:87]
	v_mfma_f32_16x16x32_bf16 v[88:91], v[76:79], v[28:31], v[88:91]
	v_mfma_f32_16x16x32_bf16 v[68:71], v[76:79], v[48:51], v[68:71]
	v_mfma_f32_16x16x32_bf16 v[76:79], v[96:99], v[4:7], v[100:103]
	v_mfma_f32_16x16x32_bf16 v[100:103], v[96:99], v[16:19], v[104:107]
	v_mfma_f32_16x16x32_bf16 v[104:107], v[96:99], v[28:31], v[108:111]
	s_nop 2
	s_nop 1
	v_mov_b32_e32 v108, v164
	v_mov_b32_e32 v109, v165
	v_mov_b32_e32 v110, v166
	v_mov_b32_e32 v111, v167
	v_mov_b32_e32 v112, v168
	v_mov_b32_e32 v113, v169
	v_mov_b32_e32 v114, v170
	v_mov_b32_e32 v115, v171
	v_mov_b32_e32 v116, v172
	v_mov_b32_e32 v117, v173
	v_mov_b32_e32 v118, v174
	v_mov_b32_e32 v119, v175
	s_nop 1
	v_mfma_f32_16x16x32_bf16 v[80:83], v[108:111], v[8:11], v[80:83]
	v_mfma_f32_16x16x32_bf16 v[84:87], v[108:111], v[20:23], v[84:87]
	v_mfma_f32_16x16x32_bf16 v[88:91], v[108:111], v[32:35], v[88:91]
	v_mfma_f32_16x16x32_bf16 v[68:71], v[108:111], v[52:55], v[68:71]
	s_nop 3
	v_mov_b32_e32 v108, v178
	v_mov_b32_e32 v109, v179
	v_mov_b32_e32 v110, v180
	v_mov_b32_e32 v111, v181
	v_add_u32_e32 v184, s90, v72
	v_min_u32_e32 v184, s68, v184
	v_lshrrev_b32_e32 v185, 3, v184
	v_lshlrev_b32_e32 v185, 17, v185
	v_and_b32_e32 v184, 7, v184
	v_lshl_or_b32 v184, v184, 9, v185
	v_mov_b32_e32 v185, 0
	v_lshl_add_u64 v[184:185], v[182:183], 0, v[184:185]
	v_mov_b32_e32 v186, 0x10000
	v_mov_b32_e32 v187, 0
	v_lshl_add_u64 v[186:187], v[184:185], 0, v[186:187]
	global_load_dwordx4 v[148:151], v[184:185], off
	global_load_dwordx4 v[152:155], v[184:185], off offset:64
	global_load_dwordx4 v[156:159], v[186:187], off
	global_load_dwordx4 v[160:163], v[186:187], off offset:64
	global_load_dwordx4 v[164:167], v[184:185], off offset:128
	global_load_dwordx4 v[168:171], v[184:185], off offset:192
	global_load_dwordx4 v[172:175], v[186:187], off offset:128
	global_load_dwordx4 v[178:181], v[186:187], off offset:192
	s_nop 1
	v_mfma_f32_16x16x32_bf16 v[80:83], v[112:115], v[12:15], v[80:83]
	v_mfma_f32_16x16x32_bf16 v[84:87], v[112:115], v[40:43], v[84:87]
	v_mfma_f32_16x16x32_bf16 v[88:91], v[112:115], v[36:39], v[88:91]
	v_mfma_f32_16x16x32_bf16 v[68:71], v[112:115], v[60:63], v[68:71]
	v_and_b32_e32 v112, 0xfffffe0, v75
	v_lshl_or_b32 v67, v67, 2, v112
	v_mul_lo_u32 v67, v67, s2
	v_add3_u32 v64, v146, v67, v64
	v_add_u32_e32 v67, 0x400, v64
	s_nop 0
	ds_write2_b32 v64, v80, v84 offset1:16
	ds_write2_b32 v64, v81, v85 offset0:132 offset1:148
	ds_write2_b32 v67, v82, v86 offset0:8 offset1:24
	ds_write2_b32 v67, v83, v87 offset0:140 offset1:156
	ds_write2_b32 v64, v88, v68 offset0:32 offset1:48
	v_mfma_f32_16x16x32_bf16 v[80:83], v[92:95], v[44:47], 0
	ds_write2_b32 v64, v89, v69 offset0:164 offset1:180
	ds_write2_b32 v67, v90, v70 offset0:40 offset1:56
	ds_write2_b32 v67, v91, v71 offset0:172 offset1:188
	v_add_u32_e32 v67, 0x2000, v64
	v_add_u32_e32 v64, 0x2400, v64
	v_mfma_f32_16x16x32_bf16 v[68:71], v[96:99], v[48:51], v[80:83]
	v_mfma_f32_16x16x32_bf16 v[76:79], v[116:119], v[8:11], v[76:79]
	v_mfma_f32_16x16x32_bf16 v[100:103], v[116:119], v[20:23], v[100:103]
	v_mfma_f32_16x16x32_bf16 v[104:107], v[116:119], v[32:35], v[104:107]
	v_mfma_f32_16x16x32_bf16 v[68:71], v[116:119], v[52:55], v[68:71]
	v_mfma_f32_16x16x32_bf16 v[76:79], v[108:111], v[12:15], v[76:79]
	v_mfma_f32_16x16x32_bf16 v[100:103], v[108:111], v[40:43], v[100:103]
	s_nop 7
	ds_write2_b32 v67, v76, v100 offset0:64 offset1:80
	ds_write2_b32 v67, v77, v101 offset0:196 offset1:212
	v_mfma_f32_16x16x32_bf16 v[104:107], v[108:111], v[36:39], v[104:107]
	ds_write2_b32 v64, v78, v102 offset0:72 offset1:88
	ds_write2_b32 v64, v79, v103 offset0:204 offset1:220
	v_mfma_f32_16x16x32_bf16 v[68:71], v[108:111], v[60:63], v[68:71]
	s_nop 7
	ds_write2_b32 v67, v104, v68 offset0:96 offset1:112
	ds_write2_b32 v67, v105, v69 offset0:228 offset1:244
	ds_write2_b32 v64, v106, v70 offset0:104 offset1:120
	ds_write2_b32 v64, v107, v71 offset0:236 offset1:252
	s_waitcnt lgkmcnt(0)
	s_barrier
; DI unsigned ordkey(float f) { const unsigned u = __float_as_uint(f); return (u & 0x80000000u) ? ~u : (u | 0x80000000u); }
; DI void peer_select_unit(const Params& p, int unit, char* lds, const bf16x8 (&kb)[4][4]) {
;     ...
; #pragma unroll 1
;   for (int pass = 0; pass < 2; ++pass) {
;     const int rr = pass * 32 + (tid >> 3), part = tid & 7;
;     unsigned a[16], bq[16];
;     const float* srow = sc + rr * 132 + 16 * part;
; #pragma unroll
;     for (int j = 0; j < 4; ++j) {
;       const f32x4 v = *(const f32x4*)(srow + 4 * j);
; #pragma unroll
;       for (int e = 0; e < 4; ++e) a[4 * j + e] = (ordkey(v[e]) & ~127u) | (unsigned)(127 - (16 * part + 4 * j + e));
;     }
	v_xor_b32_e32 v240, v249, v66
	v_cmp_gt_u32_e32 vcc, 0x80, v240
	s_and_saveexec_b64 s[8:9], vcc
	s_cbranch_execz .Lps2b_skip
	v_lshrrev_b32_e32 v236, 1, v240
	v_and_b32_e32 v237, 1, v240
	v_mul_u32_u24_e32 v238, 0x210, v236
	v_add_u32_e32 v238, v146, v238
	v_lshl_add_u32 v239, v237, 6, v238
	ds_read_b128 v[124:127], v239 offset:0
	ds_read_b128 v[128:131], v239 offset:16
	ds_read_b128 v[132:135], v239 offset:32
	ds_read_b128 v[136:139], v239 offset:48
	ds_read_b128 v[212:215], v239 offset:128
	ds_read_b128 v[216:219], v239 offset:144
	ds_read_b128 v[220:223], v239 offset:160
	ds_read_b128 v[224:227], v239 offset:176
	v_lshlrev_b32_e32 v240, 4, v237
	v_sub_u32_e32 v241, 0x7f, v240
	v_mov_b32_e32 v243, 0xffffff80
	v_bfrev_b32_e32 v242, 1
	s_waitcnt lgkmcnt(7)
	v_ashrrev_i32_e32 v122, 31, v124
	v_bitop3_b32 v124, v124, v122, v242 bitop3:0x1e
	v_and_or_b32 v124, v124, v243, v241
	v_ashrrev_i32_e32 v123, 31, v125
	v_bitop3_b32 v125, v125, v123, v242 bitop3:0x1e
	v_and_or_b32 v125, v125, v243, v241
	v_subrev_u32_e32 v125, 1, v125
	v_ashrrev_i32_e32 v144, 31, v126
	v_bitop3_b32 v126, v126, v144, v242 bitop3:0x1e
	v_and_or_b32 v126, v126, v243, v241
	v_subrev_u32_e32 v126, 2, v126
	v_ashrrev_i32_e32 v145, 31, v127
	v_bitop3_b32 v127, v127, v145, v242 bitop3:0x1e
	v_and_or_b32 v127, v127, v243, v241
	v_subrev_u32_e32 v127, 3, v127
	s_waitcnt lgkmcnt(6)
	v_ashrrev_i32_e32 v228, 31, v128
	v_bitop3_b32 v128, v128, v228, v242 bitop3:0x1e
	v_and_or_b32 v128, v128, v243, v241
	v_subrev_u32_e32 v128, 4, v128
	v_ashrrev_i32_e32 v229, 31, v129
	v_bitop3_b32 v129, v129, v229, v242 bitop3:0x1e
	v_and_or_b32 v129, v129, v243, v241
	v_subrev_u32_e32 v129, 5, v129
	v_ashrrev_i32_e32 v230, 31, v130
	v_bitop3_b32 v130, v130, v230, v242 bitop3:0x1e
	v_and_or_b32 v130, v130, v243, v241
	v_subrev_u32_e32 v130, 6, v130
	v_ashrrev_i32_e32 v231, 31, v131
	v_bitop3_b32 v131, v131, v231, v242 bitop3:0x1e
	v_and_or_b32 v131, v131, v243, v241
	v_subrev_u32_e32 v131, 7, v131
	s_waitcnt lgkmcnt(5)
	v_ashrrev_i32_e32 v232, 31, v132
	v_bitop3_b32 v132, v132, v232, v242 bitop3:0x1e
	v_and_or_b32 v132, v132, v243, v241
	v_subrev_u32_e32 v132, 8, v132
	v_ashrrev_i32_e32 v233, 31, v133
	v_bitop3_b32 v133, v133, v233, v242 bitop3:0x1e
	v_and_or_b32 v133, v133, v243, v241
	v_subrev_u32_e32 v133, 9, v133
	v_ashrrev_i32_e32 v234, 31, v134
	v_bitop3_b32 v134, v134, v234, v242 bitop3:0x1e
	v_and_or_b32 v134, v134, v243, v241
	v_subrev_u32_e32 v134, 10, v134
	v_ashrrev_i32_e32 v235, 31, v135
	v_bitop3_b32 v135, v135, v235, v242 bitop3:0x1e
	v_and_or_b32 v135, v135, v243, v241
	v_subrev_u32_e32 v135, 11, v135
	s_waitcnt lgkmcnt(4)
	v_ashrrev_i32_e32 v122, 31, v136
	v_bitop3_b32 v136, v136, v122, v242 bitop3:0x1e
	v_and_or_b32 v136, v136, v243, v241
	v_subrev_u32_e32 v136, 12, v136
	v_ashrrev_i32_e32 v123, 31, v137
	v_bitop3_b32 v137, v137, v123, v242 bitop3:0x1e
	v_and_or_b32 v137, v137, v243, v241
	v_subrev_u32_e32 v137, 13, v137
	v_ashrrev_i32_e32 v144, 31, v138
	v_bitop3_b32 v138, v138, v144, v242 bitop3:0x1e
	v_and_or_b32 v138, v138, v243, v241
	v_subrev_u32_e32 v138, 14, v138
	v_ashrrev_i32_e32 v145, 31, v139
	v_bitop3_b32 v139, v139, v145, v242 bitop3:0x1e
	v_and_or_b32 v139, v139, v243, v241
	v_subrev_u32_e32 v139, 15, v139
	s_waitcnt lgkmcnt(3)
	v_ashrrev_i32_e32 v228, 31, v212
	v_bitop3_b32 v212, v212, v228, v242 bitop3:0x1e
	v_and_or_b32 v212, v212, v243, v241
	v_subrev_u32_e32 v212, 32, v212
	v_ashrrev_i32_e32 v229, 31, v213
	v_bitop3_b32 v213, v213, v229, v242 bitop3:0x1e
	v_and_or_b32 v213, v213, v243, v241
	v_subrev_u32_e32 v213, 33, v213
	v_ashrrev_i32_e32 v230, 31, v214
	v_bitop3_b32 v214, v214, v230, v242 bitop3:0x1e
	v_and_or_b32 v214, v214, v243, v241
	v_subrev_u32_e32 v214, 34, v214
	v_ashrrev_i32_e32 v231, 31, v215
	v_bitop3_b32 v215, v215, v231, v242 bitop3:0x1e
	v_and_or_b32 v215, v215, v243, v241
	v_subrev_u32_e32 v215, 35, v215
	s_waitcnt lgkmcnt(2)
	v_ashrrev_i32_e32 v232, 31, v216
	v_bitop3_b32 v216, v216, v232, v242 bitop3:0x1e
	v_and_or_b32 v216, v216, v243, v241
	v_subrev_u32_e32 v216, 36, v216
	v_ashrrev_i32_e32 v233, 31, v217
	v_bitop3_b32 v217, v217, v233, v242 bitop3:0x1e
	v_and_or_b32 v217, v217, v243, v241
	v_subrev_u32_e32 v217, 37, v217
	v_ashrrev_i32_e32 v234, 31, v218
	v_bitop3_b32 v218, v218, v234, v242 bitop3:0x1e
	v_and_or_b32 v218, v218, v243, v241
	v_subrev_u32_e32 v218, 38, v218
	v_ashrrev_i32_e32 v235, 31, v219
	v_bitop3_b32 v219, v219, v235, v242 bitop3:0x1e
	v_and_or_b32 v219, v219, v243, v241
	v_subrev_u32_e32 v219, 39, v219
	s_waitcnt lgkmcnt(1)
	v_ashrrev_i32_e32 v122, 31, v220
	v_bitop3_b32 v220, v220, v122, v242 bitop3:0x1e
	v_and_or_b32 v220, v220, v243, v241
	v_subrev_u32_e32 v220, 40, v220
	v_ashrrev_i32_e32 v123, 31, v221
	v_bitop3_b32 v221, v221, v123, v242 bitop3:0x1e
	v_and_or_b32 v221, v221, v243, v241
	v_subrev_u32_e32 v221, 41, v221
	v_ashrrev_i32_e32 v144, 31, v222
	v_bitop3_b32 v222, v222, v144, v242 bitop3:0x1e
	v_and_or_b32 v222, v222, v243, v241
	v_subrev_u32_e32 v222, 42, v222
	v_ashrrev_i32_e32 v145, 31, v223
	v_bitop3_b32 v223, v223, v145, v242 bitop3:0x1e
	v_and_or_b32 v223, v223, v243, v241
	v_subrev_u32_e32 v223, 43, v223
	s_waitcnt lgkmcnt(0)
; DI unsigned ordkey(float f) { const unsigned u = __float_as_uint(f); return (u & 0x80000000u) ? ~u : (u | 0x80000000u); }
; #define CE_DESC(x, y) do { const unsigned mx_ = (x) > (y) ? (x) : (y); const unsigned mn_ = (x) > (y) ? (y) : (x); (x) = mx_; (y) = mn_; } while (0)
; DI void sort16_desc(unsigned (&a)[16]) {
; #pragma unroll
;   for (int k = 2; k <= 16; k <<= 1)
; #pragma unroll
;     for (int j = k >> 1; j > 0; j >>= 1)
; #pragma unroll
;       for (int i = 0; i < 16; ++i) {
;         const int l = i ^ j;
;         if (l > i) { if ((i & k) == 0) CE_DESC(a[i], a[l]); else CE_DESC(a[l], a[i]); }
;       }
; }
; DI void merge16_desc(unsigned (&a)[16], const unsigned (&b)[16]) {
; #pragma unroll
;   for (int i = 0; i < 16; ++i) a[i] = a[i] > b[15 - i] ? a[i] : b[15 - i];
; #pragma unroll
;   for (int j = 8; j > 0; j >>= 1)
; #pragma unroll
;     for (int i = 0; i < 16; ++i) if ((i & j) == 0) CE_DESC(a[i], a[i + j]);
; }
; DI void peer_select_unit(const Params& p, int unit, char* lds, const bf16x8 (&kb)[4][4]) {
;     ...
;       for (int e = 0; e < 4; ++e) a[4 * j + e] = (ordkey(v[e]) & ~127u) | (unsigned)(127 - (16 * part + 4 * j + e));
;     }
;     sort16_desc(a);
	v_ashrrev_i32_e32 v228, 31, v224
	v_bitop3_b32 v224, v224, v228, v242 bitop3:0x1e
	v_and_or_b32 v224, v224, v243, v241
	v_subrev_u32_e32 v224, 44, v224
	v_ashrrev_i32_e32 v229, 31, v225
	v_bitop3_b32 v225, v225, v229, v242 bitop3:0x1e
	v_and_or_b32 v225, v225, v243, v241
	v_subrev_u32_e32 v225, 45, v225
	v_ashrrev_i32_e32 v230, 31, v226
	v_bitop3_b32 v226, v226, v230, v242 bitop3:0x1e
	v_and_or_b32 v226, v226, v243, v241
	v_subrev_u32_e32 v226, 46, v226
	v_ashrrev_i32_e32 v231, 31, v227
	v_bitop3_b32 v227, v227, v231, v242 bitop3:0x1e
	v_and_or_b32 v227, v227, v243, v241
	v_subrev_u32_e32 v227, 47, v227
	v_max_u32_e32 v232, v124, v137
	v_min_u32_e32 v233, v124, v137
	v_max_u32_e32 v234, v212, v225
	v_min_u32_e32 v235, v212, v225
	v_max_u32_e32 v122, v125, v136
	v_min_u32_e32 v123, v125, v136
	v_max_u32_e32 v144, v213, v224
	v_min_u32_e32 v145, v213, v224
	v_max_u32_e32 v228, v126, v139
	v_min_u32_e32 v229, v126, v139
	v_max_u32_e32 v230, v214, v227
	v_min_u32_e32 v231, v214, v227
	v_max_u32_e32 v124, v127, v138
	v_min_u32_e32 v137, v127, v138
	v_max_u32_e32 v212, v215, v226
	v_min_u32_e32 v225, v215, v226
	v_max_u32_e32 v125, v128, v132
	v_min_u32_e32 v136, v128, v132
	v_max_u32_e32 v213, v216, v220
	v_min_u32_e32 v224, v216, v220
	v_max_u32_e32 v126, v129, v130
	v_min_u32_e32 v139, v129, v130
	v_max_u32_e32 v214, v217, v218
	v_min_u32_e32 v227, v217, v218
	v_max_u32_e32 v127, v131, v135
	v_min_u32_e32 v138, v131, v135
	v_max_u32_e32 v215, v219, v223
	v_min_u32_e32 v226, v219, v223
	v_max_u32_e32 v128, v133, v134
	v_min_u32_e32 v132, v133, v134
	v_max_u32_e32 v216, v221, v222
	v_min_u32_e32 v220, v221, v222
	v_max_u32_e32 v129, v232, v126
	v_min_u32_e32 v130, v232, v126
	v_max_u32_e32 v217, v234, v214
	v_min_u32_e32 v218, v234, v214
	v_max_u32_e32 v131, v122, v127
	v_min_u32_e32 v135, v122, v127
	v_max_u32_e32 v219, v144, v215
	v_min_u32_e32 v223, v144, v215
	v_max_u32_e32 v133, v228, v128
	v_min_u32_e32 v134, v228, v128
	v_max_u32_e32 v221, v230, v216
	v_min_u32_e32 v222, v230, v216
	v_max_u32_e32 v232, v124, v125
	v_min_u32_e32 v126, v124, v125
	v_max_u32_e32 v234, v212, v213
	v_min_u32_e32 v214, v212, v213
	v_max_u32_e32 v122, v139, v233
	v_min_u32_e32 v127, v139, v233
	v_max_u32_e32 v144, v227, v235
	v_min_u32_e32 v215, v227, v235
	v_max_u32_e32 v228, v136, v137
	v_min_u32_e32 v128, v136, v137
	v_max_u32_e32 v230, v224, v225
	v_min_u32_e32 v216, v224, v225
	v_max_u32_e32 v124, v132, v229
	v_min_u32_e32 v125, v132, v229
	v_max_u32_e32 v212, v220, v231
	v_min_u32_e32 v213, v220, v231
	v_max_u32_e32 v139, v138, v123
	v_min_u32_e32 v233, v138, v123
	v_max_u32_e32 v227, v226, v145
	v_min_u32_e32 v235, v226, v145
	v_max_u32_e32 v136, v129, v131
	v_min_u32_e32 v137, v129, v131
	v_max_u32_e32 v224, v217, v219
	v_min_u32_e32 v225, v217, v219
	v_max_u32_e32 v132, v133, v232
	v_min_u32_e32 v229, v133, v232
	v_max_u32_e32 v220, v221, v234
	v_min_u32_e32 v231, v221, v234
	v_max_u32_e32 v138, v126, v130
	v_min_u32_e32 v123, v126, v130
	v_max_u32_e32 v226, v214, v218
	v_min_u32_e32 v145, v214, v218
	v_max_u32_e32 v129, v122, v228
	v_min_u32_e32 v131, v122, v228
	v_max_u32_e32 v217, v144, v230
	v_min_u32_e32 v219, v144, v230
	v_max_u32_e32 v133, v135, v134
	v_min_u32_e32 v232, v135, v134
	v_max_u32_e32 v221, v223, v222
	v_min_u32_e32 v234, v223, v222
	v_max_u32_e32 v126, v124, v139
	v_min_u32_e32 v130, v124, v139
	v_max_u32_e32 v214, v212, v227
	v_min_u32_e32 v218, v212, v227
	v_max_u32_e32 v122, v233, v127
	v_min_u32_e32 v228, v233, v127
	v_max_u32_e32 v144, v235, v215
	v_min_u32_e32 v230, v235, v215
	v_max_u32_e32 v135, v128, v125
	v_min_u32_e32 v134, v128, v125
	v_max_u32_e32 v223, v216, v213
	v_min_u32_e32 v222, v216, v213
	v_max_u32_e32 v124, v136, v132
	v_min_u32_e32 v139, v136, v132
	v_max_u32_e32 v212, v224, v220
	v_min_u32_e32 v227, v224, v220
	v_max_u32_e32 v233, v137, v229
	v_min_u32_e32 v127, v137, v229
	v_max_u32_e32 v235, v225, v231
	v_min_u32_e32 v215, v225, v231
	v_max_u32_e32 v128, v138, v126
	v_min_u32_e32 v125, v138, v126
	v_max_u32_e32 v216, v226, v214
	v_min_u32_e32 v213, v226, v214
	v_max_u32_e32 v136, v123, v130
	v_min_u32_e32 v132, v123, v130
	v_max_u32_e32 v224, v145, v218
	v_min_u32_e32 v220, v145, v218
	v_max_u32_e32 v137, v129, v133
	v_min_u32_e32 v229, v129, v133
	v_max_u32_e32 v225, v217, v221
	v_min_u32_e32 v231, v217, v221
	v_max_u32_e32 v138, v131, v232
	v_min_u32_e32 v126, v131, v232
	v_max_u32_e32 v226, v219, v234
	v_min_u32_e32 v214, v219, v234
	v_max_u32_e32 v123, v122, v135
	v_min_u32_e32 v130, v122, v135
	v_max_u32_e32 v145, v144, v223
	v_min_u32_e32 v218, v144, v223
	v_max_u32_e32 v129, v228, v134
	v_min_u32_e32 v133, v228, v134
	v_max_u32_e32 v217, v230, v222
	v_min_u32_e32 v221, v230, v222
	v_max_u32_e32 v131, v233, v139
	v_min_u32_e32 v232, v233, v139
	v_max_u32_e32 v219, v235, v227
	v_min_u32_e32 v234, v235, v227
	v_max_u32_e32 v122, v127, v123
	v_min_u32_e32 v135, v127, v123
	v_max_u32_e32 v144, v215, v145
	v_min_u32_e32 v223, v215, v145
	v_max_u32_e32 v228, v128, v137
	v_min_u32_e32 v134, v128, v137
	v_max_u32_e32 v230, v216, v225
	v_min_u32_e32 v222, v216, v225
	v_max_u32_e32 v233, v136, v229
	v_min_u32_e32 v139, v136, v229
	v_max_u32_e32 v235, v224, v231
	v_min_u32_e32 v227, v224, v231
	v_max_u32_e32 v127, v138, v125
	v_min_u32_e32 v123, v138, v125
	v_max_u32_e32 v215, v226, v213
	v_min_u32_e32 v145, v226, v213
	v_max_u32_e32 v128, v126, v132
	v_min_u32_e32 v137, v126, v132
	v_max_u32_e32 v216, v214, v220
	v_min_u32_e32 v225, v214, v220
	v_max_u32_e32 v136, v129, v130
	v_min_u32_e32 v229, v129, v130
	v_max_u32_e32 v224, v217, v218
	v_min_u32_e32 v231, v217, v218
	v_max_u32_e32 v138, v131, v228
; DI unsigned ordkey(float f) { const unsigned u = __float_as_uint(f); return (u & 0x80000000u) ? ~u : (u | 0x80000000u); }
; #define CE_DESC(x, y) do { const unsigned mx_ = (x) > (y) ? (x) : (y); const unsigned mn_ = (x) > (y) ? (y) : (x); (x) = mx_; (y) = mn_; } while (0)
; DI void sort16_desc(unsigned (&a)[16]) {
; #pragma unroll
;   for (int k = 2; k <= 16; k <<= 1)
; #pragma unroll
;     for (int j = k >> 1; j > 0; j >>= 1)
; #pragma unroll
;       for (int i = 0; i < 16; ++i) {
;         const int l = i ^ j;
;         if (l > i) { if ((i & k) == 0) CE_DESC(a[i], a[l]); else CE_DESC(a[l], a[i]); }
;       }
; }
; DI void merge16_desc(unsigned (&a)[16], const unsigned (&b)[16]) {
; #pragma unroll
;   for (int i = 0; i < 16; ++i) a[i] = a[i] > b[15 - i] ? a[i] : b[15 - i];
; #pragma unroll
;   for (int j = 8; j > 0; j >>= 1)
; #pragma unroll
;     for (int i = 0; i < 16; ++i) if ((i & j) == 0) CE_DESC(a[i], a[i + j]);
; }
; DI void peer_select_unit(const Params& p, int unit, char* lds, const bf16x8 (&kb)[4][4]) {
;     ...
;     const float* srow = sc + rr * 132 + 16 * part;
; #pragma unroll
;     for (int j = 0; j < 4; ++j) {
;       const f32x4 v = *(const f32x4*)(srow + 4 * j);
; #pragma unroll
;       for (int e = 0; e < 4; ++e) a[4 * j + e] = (ordkey(v[e]) & ~127u) | (unsigned)(127 - (16 * part + 4 * j + e));
;     }
	v_min_u32_e32 v125, v131, v228
	v_max_u32_e32 v226, v219, v230
	v_min_u32_e32 v213, v219, v230
	v_max_u32_e32 v126, v232, v134
	v_min_u32_e32 v132, v232, v134
	v_max_u32_e32 v214, v234, v222
	v_min_u32_e32 v220, v234, v222
	v_max_u32_e32 v129, v233, v127
	v_min_u32_e32 v130, v233, v127
	v_max_u32_e32 v217, v235, v215
	v_min_u32_e32 v218, v235, v215
	v_max_u32_e32 v131, v139, v123
	v_min_u32_e32 v228, v139, v123
	v_max_u32_e32 v219, v227, v145
	v_min_u32_e32 v230, v227, v145
	v_max_u32_e32 v232, v128, v136
	v_min_u32_e32 v134, v128, v136
	v_max_u32_e32 v234, v216, v224
	v_min_u32_e32 v222, v216, v224
	v_max_u32_e32 v233, v137, v229
	v_min_u32_e32 v127, v137, v229
	v_max_u32_e32 v235, v225, v231
	v_min_u32_e32 v215, v225, v231
	v_max_u32_e32 v139, v126, v125
	v_min_u32_e32 v123, v126, v125
	v_max_u32_e32 v227, v214, v213
	v_min_u32_e32 v145, v214, v213
	v_max_u32_e32 v128, v122, v132
	v_min_u32_e32 v136, v122, v132
	v_max_u32_e32 v216, v144, v220
	v_min_u32_e32 v224, v144, v220
	v_max_u32_e32 v137, v232, v135
	v_min_u32_e32 v229, v232, v135
	v_max_u32_e32 v225, v234, v223
	v_min_u32_e32 v231, v234, v223
	v_max_u32_e32 v126, v233, v134
	v_min_u32_e32 v125, v233, v134
	v_max_u32_e32 v214, v235, v222
	v_min_u32_e32 v213, v235, v222
	v_max_u32_e32 v122, v128, v129
	v_min_u32_e32 v132, v128, v129
	v_max_u32_e32 v144, v216, v217
	v_min_u32_e32 v220, v216, v217
	v_max_u32_e32 v232, v136, v130
	v_min_u32_e32 v135, v136, v130
	v_max_u32_e32 v234, v224, v218
	v_min_u32_e32 v223, v224, v218
	v_max_u32_e32 v233, v131, v137
	v_min_u32_e32 v134, v131, v137
	v_max_u32_e32 v235, v219, v225
	v_min_u32_e32 v222, v219, v225
	v_max_u32_e32 v128, v228, v229
	v_min_u32_e32 v129, v228, v229
	v_max_u32_e32 v216, v230, v231
	v_min_u32_e32 v217, v230, v231
	v_max_u32_e32 v136, v122, v123
	v_min_u32_e32 v130, v122, v123
	v_max_u32_e32 v224, v144, v145
	v_min_u32_e32 v218, v144, v145
	v_max_u32_e32 v131, v132, v232
	v_min_u32_e32 v137, v132, v232
	v_max_u32_e32 v219, v220, v234
	v_min_u32_e32 v225, v220, v234
	v_max_u32_e32 v228, v233, v135
	v_min_u32_e32 v229, v233, v135
	v_max_u32_e32 v230, v235, v223
	v_min_u32_e32 v231, v235, v223
	v_max_u32_e32 v122, v134, v128
	v_min_u32_e32 v123, v134, v128
	v_max_u32_e32 v144, v222, v216
	v_min_u32_e32 v145, v222, v216
	v_max_u32_e32 v132, v126, v129
	v_min_u32_e32 v232, v126, v129
	v_max_u32_e32 v220, v214, v217
	v_min_u32_e32 v234, v214, v217
	v_max_u32_e32 v233, v137, v228
	v_min_u32_e32 v135, v137, v228
	v_max_u32_e32 v235, v225, v230
	v_min_u32_e32 v223, v225, v230
	v_max_u32_e32 v134, v229, v122
	v_min_u32_e32 v128, v229, v122
	v_max_u32_e32 v222, v231, v144
	v_min_u32_e32 v216, v231, v144
	v_max_u32_e32 v126, v124, v221
	v_max_u32_e32 v129, v138, v215
	v_max_u32_e32 v214, v139, v213
	v_max_u32_e32 v217, v136, v234
	v_max_u32_e32 v137, v130, v220
	v_max_u32_e32 v228, v131, v145
	v_max_u32_e32 v225, v233, v216
	v_max_u32_e32 v230, v135, v222
	v_max_u32_e32 v229, v134, v223
	v_max_u32_e32 v122, v128, v235
	v_max_u32_e32 v231, v123, v219
	v_max_u32_e32 v144, v132, v218
	v_max_u32_e32 v124, v232, v224
	v_max_u32_e32 v138, v125, v227
	v_max_u32_e32 v139, v127, v226
	v_max_u32_e32 v136, v133, v212
	v_max_u32_e32 v130, v126, v229
	v_min_u32_e32 v131, v126, v229
	v_max_u32_e32 v233, v129, v122
	v_min_u32_e32 v135, v129, v122
	v_max_u32_e32 v134, v214, v231
	v_min_u32_e32 v128, v214, v231
	v_max_u32_e32 v123, v217, v144
	v_min_u32_e32 v132, v217, v144
	v_max_u32_e32 v232, v137, v124
	v_min_u32_e32 v125, v137, v124
	v_max_u32_e32 v127, v228, v138
	v_min_u32_e32 v133, v228, v138
	v_max_u32_e32 v212, v225, v139
	v_min_u32_e32 v226, v225, v139
	v_max_u32_e32 v227, v230, v136
	v_min_u32_e32 v224, v230, v136
	v_max_u32_e32 v218, v130, v232
	v_min_u32_e32 v219, v130, v232
	v_max_u32_e32 v235, v233, v127
	v_min_u32_e32 v223, v233, v127
	v_max_u32_e32 v222, v134, v212
	v_min_u32_e32 v216, v134, v212
	v_max_u32_e32 v145, v123, v227
	v_min_u32_e32 v220, v123, v227
	v_max_u32_e32 v234, v131, v125
	v_min_u32_e32 v213, v131, v125
	v_max_u32_e32 v215, v135, v133
	v_min_u32_e32 v221, v135, v133
	v_max_u32_e32 v126, v128, v226
	v_min_u32_e32 v229, v128, v226
	v_max_u32_e32 v129, v132, v224
	v_min_u32_e32 v122, v132, v224
	v_max_u32_e32 v214, v218, v222
	v_min_u32_e32 v231, v218, v222
	v_max_u32_e32 v217, v235, v145
	v_min_u32_e32 v144, v235, v145
	v_max_u32_e32 v137, v219, v216
	v_min_u32_e32 v124, v219, v216
	v_max_u32_e32 v228, v223, v220
	v_min_u32_e32 v138, v223, v220
	v_max_u32_e32 v225, v234, v126
	v_min_u32_e32 v139, v234, v126
	v_max_u32_e32 v230, v215, v129
	v_min_u32_e32 v136, v215, v129
	v_max_u32_e32 v130, v213, v229
	v_min_u32_e32 v232, v213, v229
	v_max_u32_e32 v233, v221, v122
	v_min_u32_e32 v127, v221, v122
	v_max_u32_e32 v134, v214, v217
	v_min_u32_e32 v212, v214, v217
	v_max_u32_e32 v123, v231, v144
	v_min_u32_e32 v227, v231, v144
	v_max_u32_e32 v131, v137, v228
	v_min_u32_e32 v125, v137, v228
	v_max_u32_e32 v135, v124, v138
	v_min_u32_e32 v133, v124, v138
	v_max_u32_e32 v128, v225, v230
	v_min_u32_e32 v226, v225, v230
	v_max_u32_e32 v132, v139, v136
	v_min_u32_e32 v224, v139, v136
	v_max_u32_e32 v218, v130, v233
	v_min_u32_e32 v222, v130, v233
	v_max_u32_e32 v235, v232, v127
	v_min_u32_e32 v145, v232, v127
	v_mov_b32_e32 v194, v134
	v_mov_b32_e32 v195, v212
	v_mov_b32_e32 v196, v123
	v_mov_b32_e32 v197, v227
	v_mov_b32_e32 v198, v131
	v_mov_b32_e32 v199, v125
	v_mov_b32_e32 v200, v135
	v_mov_b32_e32 v201, v133
	v_mov_b32_e32 v202, v128
	v_mov_b32_e32 v203, v226
	v_mov_b32_e32 v204, v132
	v_mov_b32_e32 v205, v224
	v_mov_b32_e32 v140, v218
	v_mov_b32_e32 v141, v222
	v_mov_b32_e32 v142, v235
	v_mov_b32_e32 v143, v145
	ds_read_b128 v[124:127], v239 offset:256
	ds_read_b128 v[128:131], v239 offset:272
	ds_read_b128 v[132:135], v239 offset:288
	ds_read_b128 v[136:139], v239 offset:304
	ds_read_b128 v[212:215], v239 offset:384
	ds_read_b128 v[216:219], v239 offset:400
	ds_read_b128 v[220:223], v239 offset:416
	ds_read_b128 v[224:227], v239 offset:432
	s_waitcnt lgkmcnt(7)
; DI unsigned ordkey(float f) { const unsigned u = __float_as_uint(f); return (u & 0x80000000u) ? ~u : (u | 0x80000000u); }
; DI void peer_select_unit(const Params& p, int unit, char* lds, const bf16x8 (&kb)[4][4]) {
;     ...
;     const float* srow = sc + rr * 132 + 16 * part;
; #pragma unroll
;     for (int j = 0; j < 4; ++j) {
;       const f32x4 v = *(const f32x4*)(srow + 4 * j);
; #pragma unroll
;       for (int e = 0; e < 4; ++e) a[4 * j + e] = (ordkey(v[e]) & ~127u) | (unsigned)(127 - (16 * part + 4 * j + e));
;     }
	v_ashrrev_i32_e32 v122, 31, v124
	v_bitop3_b32 v124, v124, v122, v242 bitop3:0x1e
	v_and_or_b32 v124, v124, v243, v241
	v_subrev_u32_e32 v124, 64, v124
	v_ashrrev_i32_e32 v123, 31, v125
	v_bitop3_b32 v125, v125, v123, v242 bitop3:0x1e
	v_and_or_b32 v125, v125, v243, v241
	v_subrev_u32_e32 v125, 0x41, v125
	v_ashrrev_i32_e32 v144, 31, v126
	v_bitop3_b32 v126, v126, v144, v242 bitop3:0x1e
	v_and_or_b32 v126, v126, v243, v241
	v_subrev_u32_e32 v126, 0x42, v126
	v_ashrrev_i32_e32 v145, 31, v127
	v_bitop3_b32 v127, v127, v145, v242 bitop3:0x1e
	v_and_or_b32 v127, v127, v243, v241
	v_subrev_u32_e32 v127, 0x43, v127
	s_waitcnt lgkmcnt(6)
	v_ashrrev_i32_e32 v228, 31, v128
	v_bitop3_b32 v128, v128, v228, v242 bitop3:0x1e
	v_and_or_b32 v128, v128, v243, v241
	v_subrev_u32_e32 v128, 0x44, v128
	v_ashrrev_i32_e32 v229, 31, v129
	v_bitop3_b32 v129, v129, v229, v242 bitop3:0x1e
	v_and_or_b32 v129, v129, v243, v241
	v_subrev_u32_e32 v129, 0x45, v129
	v_ashrrev_i32_e32 v230, 31, v130
	v_bitop3_b32 v130, v130, v230, v242 bitop3:0x1e
	v_and_or_b32 v130, v130, v243, v241
	v_subrev_u32_e32 v130, 0x46, v130
	v_ashrrev_i32_e32 v231, 31, v131
	v_bitop3_b32 v131, v131, v231, v242 bitop3:0x1e
	v_and_or_b32 v131, v131, v243, v241
	v_subrev_u32_e32 v131, 0x47, v131
	s_waitcnt lgkmcnt(5)
	v_ashrrev_i32_e32 v232, 31, v132
	v_bitop3_b32 v132, v132, v232, v242 bitop3:0x1e
	v_and_or_b32 v132, v132, v243, v241
	v_subrev_u32_e32 v132, 0x48, v132
	v_ashrrev_i32_e32 v233, 31, v133
	v_bitop3_b32 v133, v133, v233, v242 bitop3:0x1e
	v_and_or_b32 v133, v133, v243, v241
	v_subrev_u32_e32 v133, 0x49, v133
	v_ashrrev_i32_e32 v234, 31, v134
	v_bitop3_b32 v134, v134, v234, v242 bitop3:0x1e
	v_and_or_b32 v134, v134, v243, v241
	v_subrev_u32_e32 v134, 0x4a, v134
	v_ashrrev_i32_e32 v235, 31, v135
	v_bitop3_b32 v135, v135, v235, v242 bitop3:0x1e
	v_and_or_b32 v135, v135, v243, v241
	v_subrev_u32_e32 v135, 0x4b, v135
	s_waitcnt lgkmcnt(4)
	v_ashrrev_i32_e32 v122, 31, v136
	v_bitop3_b32 v136, v136, v122, v242 bitop3:0x1e
	v_and_or_b32 v136, v136, v243, v241
	v_subrev_u32_e32 v136, 0x4c, v136
	v_ashrrev_i32_e32 v123, 31, v137
	v_bitop3_b32 v137, v137, v123, v242 bitop3:0x1e
	v_and_or_b32 v137, v137, v243, v241
	v_subrev_u32_e32 v137, 0x4d, v137
	v_ashrrev_i32_e32 v144, 31, v138
	v_bitop3_b32 v138, v138, v144, v242 bitop3:0x1e
	v_and_or_b32 v138, v138, v243, v241
	v_subrev_u32_e32 v138, 0x4e, v138
	v_ashrrev_i32_e32 v145, 31, v139
	v_bitop3_b32 v139, v139, v145, v242 bitop3:0x1e
	v_and_or_b32 v139, v139, v243, v241
	v_subrev_u32_e32 v139, 0x4f, v139
	s_waitcnt lgkmcnt(3)
	v_ashrrev_i32_e32 v228, 31, v212
	v_bitop3_b32 v212, v212, v228, v242 bitop3:0x1e
	v_and_or_b32 v212, v212, v243, v241
	v_subrev_u32_e32 v212, 0x60, v212
	v_ashrrev_i32_e32 v229, 31, v213
	v_bitop3_b32 v213, v213, v229, v242 bitop3:0x1e
	v_and_or_b32 v213, v213, v243, v241
	v_subrev_u32_e32 v213, 0x61, v213
	v_ashrrev_i32_e32 v230, 31, v214
	v_bitop3_b32 v214, v214, v230, v242 bitop3:0x1e
	v_and_or_b32 v214, v214, v243, v241
	v_subrev_u32_e32 v214, 0x62, v214
	v_ashrrev_i32_e32 v231, 31, v215
	v_bitop3_b32 v215, v215, v231, v242 bitop3:0x1e
	v_and_or_b32 v215, v215, v243, v241
	v_subrev_u32_e32 v215, 0x63, v215
	s_waitcnt lgkmcnt(2)
	v_ashrrev_i32_e32 v232, 31, v216
	v_bitop3_b32 v216, v216, v232, v242 bitop3:0x1e
	v_and_or_b32 v216, v216, v243, v241
	v_subrev_u32_e32 v216, 0x64, v216
	v_ashrrev_i32_e32 v233, 31, v217
	v_bitop3_b32 v217, v217, v233, v242 bitop3:0x1e
	v_and_or_b32 v217, v217, v243, v241
	v_subrev_u32_e32 v217, 0x65, v217
	v_ashrrev_i32_e32 v234, 31, v218
	v_bitop3_b32 v218, v218, v234, v242 bitop3:0x1e
	v_and_or_b32 v218, v218, v243, v241
	v_subrev_u32_e32 v218, 0x66, v218
	v_ashrrev_i32_e32 v235, 31, v219
	v_bitop3_b32 v219, v219, v235, v242 bitop3:0x1e
	v_and_or_b32 v219, v219, v243, v241
	v_subrev_u32_e32 v219, 0x67, v219
	s_waitcnt lgkmcnt(1)
	v_ashrrev_i32_e32 v122, 31, v220
	v_bitop3_b32 v220, v220, v122, v242 bitop3:0x1e
	v_and_or_b32 v220, v220, v243, v241
	v_subrev_u32_e32 v220, 0x68, v220
	v_ashrrev_i32_e32 v123, 31, v221
	v_bitop3_b32 v221, v221, v123, v242 bitop3:0x1e
	v_and_or_b32 v221, v221, v243, v241
	v_subrev_u32_e32 v221, 0x69, v221
	v_ashrrev_i32_e32 v144, 31, v222
	v_bitop3_b32 v222, v222, v144, v242 bitop3:0x1e
	v_and_or_b32 v222, v222, v243, v241
	v_subrev_u32_e32 v222, 0x6a, v222
	v_ashrrev_i32_e32 v145, 31, v223
	v_bitop3_b32 v223, v223, v145, v242 bitop3:0x1e
	v_and_or_b32 v223, v223, v243, v241
	v_subrev_u32_e32 v223, 0x6b, v223
	s_waitcnt lgkmcnt(0)
; #define CE_DESC(x, y) do { const unsigned mx_ = (x) > (y) ? (x) : (y); const unsigned mn_ = (x) > (y) ? (y) : (x); (x) = mx_; (y) = mn_; } while (0)
; DI void sort16_desc(unsigned (&a)[16]) {
; #pragma unroll
;   for (int k = 2; k <= 16; k <<= 1)
; #pragma unroll
;     for (int j = k >> 1; j > 0; j >>= 1)
; #pragma unroll
;       for (int i = 0; i < 16; ++i) {
;         const int l = i ^ j;
;         if (l > i) { if ((i & k) == 0) CE_DESC(a[i], a[l]); else CE_DESC(a[l], a[i]); }
;       }
; }
	v_ashrrev_i32_e32 v228, 31, v224
	v_bitop3_b32 v224, v224, v228, v242 bitop3:0x1e
	v_and_or_b32 v224, v224, v243, v241
	v_subrev_u32_e32 v224, 0x6c, v224
	v_ashrrev_i32_e32 v229, 31, v225
	v_bitop3_b32 v225, v225, v229, v242 bitop3:0x1e
	v_and_or_b32 v225, v225, v243, v241
	v_subrev_u32_e32 v225, 0x6d, v225
	v_ashrrev_i32_e32 v230, 31, v226
	v_bitop3_b32 v226, v226, v230, v242 bitop3:0x1e
	v_and_or_b32 v226, v226, v243, v241
	v_subrev_u32_e32 v226, 0x6e, v226
	v_ashrrev_i32_e32 v231, 31, v227
	v_bitop3_b32 v227, v227, v231, v242 bitop3:0x1e
	v_and_or_b32 v227, v227, v243, v241
	v_subrev_u32_e32 v227, 0x6f, v227
	v_max_u32_e32 v232, v124, v137
	v_min_u32_e32 v233, v124, v137
	v_max_u32_e32 v234, v212, v225
	v_min_u32_e32 v235, v212, v225
	v_max_u32_e32 v122, v125, v136
	v_min_u32_e32 v123, v125, v136
	v_max_u32_e32 v144, v213, v224
	v_min_u32_e32 v145, v213, v224
	v_max_u32_e32 v228, v126, v139
	v_min_u32_e32 v229, v126, v139
	v_max_u32_e32 v230, v214, v227
	v_min_u32_e32 v231, v214, v227
	v_max_u32_e32 v124, v127, v138
	v_min_u32_e32 v137, v127, v138
	v_max_u32_e32 v212, v215, v226
	v_min_u32_e32 v225, v215, v226
	v_max_u32_e32 v125, v128, v132
	v_min_u32_e32 v136, v128, v132
	v_max_u32_e32 v213, v216, v220
	v_min_u32_e32 v224, v216, v220
	v_max_u32_e32 v126, v129, v130
	v_min_u32_e32 v139, v129, v130
	v_max_u32_e32 v214, v217, v218
	v_min_u32_e32 v227, v217, v218
	v_max_u32_e32 v127, v131, v135
	v_min_u32_e32 v138, v131, v135
	v_max_u32_e32 v215, v219, v223
	v_min_u32_e32 v226, v219, v223
	v_max_u32_e32 v128, v133, v134
	v_min_u32_e32 v132, v133, v134
	v_max_u32_e32 v216, v221, v222
	v_min_u32_e32 v220, v221, v222
	v_max_u32_e32 v129, v232, v126
	v_min_u32_e32 v130, v232, v126
	v_max_u32_e32 v217, v234, v214
	v_min_u32_e32 v218, v234, v214
	v_max_u32_e32 v131, v122, v127
	v_min_u32_e32 v135, v122, v127
	v_max_u32_e32 v219, v144, v215
	v_min_u32_e32 v223, v144, v215
	v_max_u32_e32 v133, v228, v128
	v_min_u32_e32 v134, v228, v128
	v_max_u32_e32 v221, v230, v216
	v_min_u32_e32 v222, v230, v216
	v_max_u32_e32 v232, v124, v125
	v_min_u32_e32 v126, v124, v125
	v_max_u32_e32 v234, v212, v213
	v_min_u32_e32 v214, v212, v213
	v_max_u32_e32 v122, v139, v233
	v_min_u32_e32 v127, v139, v233
	v_max_u32_e32 v144, v227, v235
	v_min_u32_e32 v215, v227, v235
	v_max_u32_e32 v228, v136, v137
	v_min_u32_e32 v128, v136, v137
	v_max_u32_e32 v230, v224, v225
	v_min_u32_e32 v216, v224, v225
	v_max_u32_e32 v124, v132, v229
	v_min_u32_e32 v125, v132, v229
	v_max_u32_e32 v212, v220, v231
	v_min_u32_e32 v213, v220, v231
	v_max_u32_e32 v139, v138, v123
	v_min_u32_e32 v233, v138, v123
	v_max_u32_e32 v227, v226, v145
	v_min_u32_e32 v235, v226, v145
	v_max_u32_e32 v136, v129, v131
	v_min_u32_e32 v137, v129, v131
	v_max_u32_e32 v224, v217, v219
	v_min_u32_e32 v225, v217, v219
	v_max_u32_e32 v132, v133, v232
	v_min_u32_e32 v229, v133, v232
	v_max_u32_e32 v220, v221, v234
	v_min_u32_e32 v231, v221, v234
	v_max_u32_e32 v138, v126, v130
	v_min_u32_e32 v123, v126, v130
	v_max_u32_e32 v226, v214, v218
	v_min_u32_e32 v145, v214, v218
	v_max_u32_e32 v129, v122, v228
	v_min_u32_e32 v131, v122, v228
	v_max_u32_e32 v217, v144, v230
	v_min_u32_e32 v219, v144, v230
	v_max_u32_e32 v133, v135, v134
	v_min_u32_e32 v232, v135, v134
	v_max_u32_e32 v221, v223, v222
	v_min_u32_e32 v234, v223, v222
	v_max_u32_e32 v126, v124, v139
	v_min_u32_e32 v130, v124, v139
	v_max_u32_e32 v214, v212, v227
	v_min_u32_e32 v218, v212, v227
	v_max_u32_e32 v122, v233, v127
	v_min_u32_e32 v228, v233, v127
	v_max_u32_e32 v144, v235, v215
	v_min_u32_e32 v230, v235, v215
	v_max_u32_e32 v135, v128, v125
	v_min_u32_e32 v134, v128, v125
	v_max_u32_e32 v223, v216, v213
	v_min_u32_e32 v222, v216, v213
	v_max_u32_e32 v124, v136, v132
	v_min_u32_e32 v139, v136, v132
	v_max_u32_e32 v212, v224, v220
	v_min_u32_e32 v227, v224, v220
	v_max_u32_e32 v233, v137, v229
	v_min_u32_e32 v127, v137, v229
	v_max_u32_e32 v235, v225, v231
	v_min_u32_e32 v215, v225, v231
	v_max_u32_e32 v128, v138, v126
	v_min_u32_e32 v125, v138, v126
	v_max_u32_e32 v216, v226, v214
	v_min_u32_e32 v213, v226, v214
	v_max_u32_e32 v136, v123, v130
	v_min_u32_e32 v132, v123, v130
	v_max_u32_e32 v224, v145, v218
	v_min_u32_e32 v220, v145, v218
	v_max_u32_e32 v137, v129, v133
	v_min_u32_e32 v229, v129, v133
	v_max_u32_e32 v225, v217, v221
	v_min_u32_e32 v231, v217, v221
	v_max_u32_e32 v138, v131, v232
	v_min_u32_e32 v126, v131, v232
	v_max_u32_e32 v226, v219, v234
	v_min_u32_e32 v214, v219, v234
	v_max_u32_e32 v123, v122, v135
	v_min_u32_e32 v130, v122, v135
	v_max_u32_e32 v145, v144, v223
	v_min_u32_e32 v218, v144, v223
	v_max_u32_e32 v129, v228, v134
	v_min_u32_e32 v133, v228, v134
	v_max_u32_e32 v217, v230, v222
	v_min_u32_e32 v221, v230, v222
	v_max_u32_e32 v131, v233, v139
	v_min_u32_e32 v232, v233, v139
	v_max_u32_e32 v219, v235, v227
	v_min_u32_e32 v234, v235, v227
	v_max_u32_e32 v122, v127, v123
	v_min_u32_e32 v135, v127, v123
	v_max_u32_e32 v144, v215, v145
	v_min_u32_e32 v223, v215, v145
	v_max_u32_e32 v228, v128, v137
	v_min_u32_e32 v134, v128, v137
	v_max_u32_e32 v230, v216, v225
	v_min_u32_e32 v222, v216, v225
	v_max_u32_e32 v233, v136, v229
	v_min_u32_e32 v139, v136, v229
	v_max_u32_e32 v235, v224, v231
	v_min_u32_e32 v227, v224, v231
	v_max_u32_e32 v127, v138, v125
	v_min_u32_e32 v123, v138, v125
	v_max_u32_e32 v215, v226, v213
	v_min_u32_e32 v145, v226, v213
	v_max_u32_e32 v128, v126, v132
	v_min_u32_e32 v137, v126, v132
	v_max_u32_e32 v216, v214, v220
	v_min_u32_e32 v225, v214, v220
	v_max_u32_e32 v136, v129, v130
	v_min_u32_e32 v229, v129, v130
	v_max_u32_e32 v224, v217, v218
	v_min_u32_e32 v231, v217, v218
	v_max_u32_e32 v138, v131, v228
; #define CE_DESC(x, y) do { const unsigned mx_ = (x) > (y) ? (x) : (y); const unsigned mn_ = (x) > (y) ? (y) : (x); (x) = mx_; (y) = mn_; } while (0)
; DI void sort16_desc(unsigned (&a)[16]) {
; #pragma unroll
;   for (int k = 2; k <= 16; k <<= 1)
; #pragma unroll
;     for (int j = k >> 1; j > 0; j >>= 1)
; #pragma unroll
;       for (int i = 0; i < 16; ++i) {
;         const int l = i ^ j;
;         if (l > i) { if ((i & k) == 0) CE_DESC(a[i], a[l]); else CE_DESC(a[l], a[i]); }
;       }
; }
; DI void merge16_desc(unsigned (&a)[16], const unsigned (&b)[16]) {
; #pragma unroll
;   for (int i = 0; i < 16; ++i) a[i] = a[i] > b[15 - i] ? a[i] : b[15 - i];
; #pragma unroll
;   for (int j = 8; j > 0; j >>= 1)
; #pragma unroll
;     for (int i = 0; i < 16; ++i) if ((i & j) == 0) CE_DESC(a[i], a[i + j]);
; }
	v_min_u32_e32 v125, v131, v228
	v_max_u32_e32 v226, v219, v230
	v_min_u32_e32 v213, v219, v230
	v_max_u32_e32 v126, v232, v134
	v_min_u32_e32 v132, v232, v134
	v_max_u32_e32 v214, v234, v222
	v_min_u32_e32 v220, v234, v222
	v_max_u32_e32 v129, v233, v127
	v_min_u32_e32 v130, v233, v127
	v_max_u32_e32 v217, v235, v215
	v_min_u32_e32 v218, v235, v215
	v_max_u32_e32 v131, v139, v123
	v_min_u32_e32 v228, v139, v123
	v_max_u32_e32 v219, v227, v145
	v_min_u32_e32 v230, v227, v145
	v_max_u32_e32 v232, v128, v136
	v_min_u32_e32 v134, v128, v136
	v_max_u32_e32 v234, v216, v224
	v_min_u32_e32 v222, v216, v224
	v_max_u32_e32 v233, v137, v229
	v_min_u32_e32 v127, v137, v229
	v_max_u32_e32 v235, v225, v231
	v_min_u32_e32 v215, v225, v231
	v_max_u32_e32 v139, v126, v125
	v_min_u32_e32 v123, v126, v125
	v_max_u32_e32 v227, v214, v213
	v_min_u32_e32 v145, v214, v213
	v_max_u32_e32 v128, v122, v132
	v_min_u32_e32 v136, v122, v132
	v_max_u32_e32 v216, v144, v220
	v_min_u32_e32 v224, v144, v220
	v_max_u32_e32 v137, v232, v135
	v_min_u32_e32 v229, v232, v135
	v_max_u32_e32 v225, v234, v223
	v_min_u32_e32 v231, v234, v223
	v_max_u32_e32 v126, v233, v134
	v_min_u32_e32 v125, v233, v134
	v_max_u32_e32 v214, v235, v222
	v_min_u32_e32 v213, v235, v222
	v_max_u32_e32 v122, v128, v129
	v_min_u32_e32 v132, v128, v129
	v_max_u32_e32 v144, v216, v217
	v_min_u32_e32 v220, v216, v217
	v_max_u32_e32 v232, v136, v130
	v_min_u32_e32 v135, v136, v130
	v_max_u32_e32 v234, v224, v218
	v_min_u32_e32 v223, v224, v218
	v_max_u32_e32 v233, v131, v137
	v_min_u32_e32 v134, v131, v137
	v_max_u32_e32 v235, v219, v225
	v_min_u32_e32 v222, v219, v225
	v_max_u32_e32 v128, v228, v229
	v_min_u32_e32 v129, v228, v229
	v_max_u32_e32 v216, v230, v231
	v_min_u32_e32 v217, v230, v231
	v_max_u32_e32 v136, v122, v123
	v_min_u32_e32 v130, v122, v123
	v_max_u32_e32 v224, v144, v145
	v_min_u32_e32 v218, v144, v145
	v_max_u32_e32 v131, v132, v232
	v_min_u32_e32 v137, v132, v232
	v_max_u32_e32 v219, v220, v234
	v_min_u32_e32 v225, v220, v234
	v_max_u32_e32 v228, v233, v135
	v_min_u32_e32 v229, v233, v135
	v_max_u32_e32 v230, v235, v223
	v_min_u32_e32 v231, v235, v223
	v_max_u32_e32 v122, v134, v128
	v_min_u32_e32 v123, v134, v128
	v_max_u32_e32 v144, v222, v216
	v_min_u32_e32 v145, v222, v216
	v_max_u32_e32 v132, v126, v129
	v_min_u32_e32 v232, v126, v129
	v_max_u32_e32 v220, v214, v217
	v_min_u32_e32 v234, v214, v217
	v_max_u32_e32 v233, v137, v228
	v_min_u32_e32 v135, v137, v228
	v_max_u32_e32 v235, v225, v230
	v_min_u32_e32 v223, v225, v230
	v_max_u32_e32 v134, v229, v122
	v_min_u32_e32 v128, v229, v122
	v_max_u32_e32 v222, v231, v144
	v_min_u32_e32 v216, v231, v144
	v_max_u32_e32 v126, v124, v221
	v_max_u32_e32 v129, v138, v215
	v_max_u32_e32 v214, v139, v213
	v_max_u32_e32 v217, v136, v234
	v_max_u32_e32 v137, v130, v220
	v_max_u32_e32 v228, v131, v145
	v_max_u32_e32 v225, v233, v216
	v_max_u32_e32 v230, v135, v222
	v_max_u32_e32 v229, v134, v223
	v_max_u32_e32 v122, v128, v235
	v_max_u32_e32 v231, v123, v219
	v_max_u32_e32 v144, v132, v218
	v_max_u32_e32 v124, v232, v224
	v_max_u32_e32 v138, v125, v227
	v_max_u32_e32 v139, v127, v226
	v_max_u32_e32 v136, v133, v212
	v_max_u32_e32 v130, v126, v229
	v_min_u32_e32 v131, v126, v229
	v_max_u32_e32 v233, v129, v122
	v_min_u32_e32 v135, v129, v122
	v_max_u32_e32 v134, v214, v231
	v_min_u32_e32 v128, v214, v231
	v_max_u32_e32 v123, v217, v144
	v_min_u32_e32 v132, v217, v144
	v_max_u32_e32 v232, v137, v124
	v_min_u32_e32 v125, v137, v124
	v_max_u32_e32 v127, v228, v138
	v_min_u32_e32 v133, v228, v138
	v_max_u32_e32 v212, v225, v139
	v_min_u32_e32 v226, v225, v139
	v_max_u32_e32 v227, v230, v136
	v_min_u32_e32 v224, v230, v136
	v_max_u32_e32 v218, v130, v232
	v_min_u32_e32 v219, v130, v232
	v_max_u32_e32 v235, v233, v127
	v_min_u32_e32 v223, v233, v127
	v_max_u32_e32 v222, v134, v212
	v_min_u32_e32 v216, v134, v212
	v_max_u32_e32 v145, v123, v227
	v_min_u32_e32 v220, v123, v227
	v_max_u32_e32 v234, v131, v125
	v_min_u32_e32 v213, v131, v125
	v_max_u32_e32 v215, v135, v133
	v_min_u32_e32 v221, v135, v133
	v_max_u32_e32 v126, v128, v226
	v_min_u32_e32 v229, v128, v226
	v_max_u32_e32 v129, v132, v224
	v_min_u32_e32 v122, v132, v224
	v_max_u32_e32 v214, v218, v222
	v_min_u32_e32 v231, v218, v222
	v_max_u32_e32 v217, v235, v145
	v_min_u32_e32 v144, v235, v145
	v_max_u32_e32 v137, v219, v216
	v_min_u32_e32 v124, v219, v216
	v_max_u32_e32 v228, v223, v220
	v_min_u32_e32 v138, v223, v220
	v_max_u32_e32 v225, v234, v126
	v_min_u32_e32 v139, v234, v126
	v_max_u32_e32 v230, v215, v129
	v_min_u32_e32 v136, v215, v129
	v_max_u32_e32 v130, v213, v229
	v_min_u32_e32 v232, v213, v229
	v_max_u32_e32 v233, v221, v122
	v_min_u32_e32 v127, v221, v122
	v_max_u32_e32 v134, v214, v217
	v_min_u32_e32 v212, v214, v217
	v_max_u32_e32 v123, v231, v144
	v_min_u32_e32 v227, v231, v144
	v_max_u32_e32 v131, v137, v228
	v_min_u32_e32 v125, v137, v228
	v_max_u32_e32 v135, v124, v138
	v_min_u32_e32 v133, v124, v138
	v_max_u32_e32 v128, v225, v230
	v_min_u32_e32 v226, v225, v230
	v_max_u32_e32 v132, v139, v136
	v_min_u32_e32 v224, v139, v136
	v_max_u32_e32 v218, v130, v233
	v_min_u32_e32 v222, v130, v233
	v_max_u32_e32 v235, v232, v127
	v_min_u32_e32 v145, v232, v127
	v_max_u32_e32 v219, v134, v143
	v_max_u32_e32 v216, v212, v142
	v_max_u32_e32 v223, v123, v141
	v_max_u32_e32 v220, v227, v140
	v_max_u32_e32 v234, v131, v205
	v_max_u32_e32 v126, v125, v204
	v_max_u32_e32 v215, v135, v203
	v_max_u32_e32 v129, v133, v202
	v_max_u32_e32 v213, v128, v201
	v_max_u32_e32 v229, v226, v200
	v_max_u32_e32 v221, v132, v199
	v_max_u32_e32 v122, v224, v198
	v_max_u32_e32 v214, v218, v197
; #define CE_DESC(x, y) do { const unsigned mx_ = (x) > (y) ? (x) : (y); const unsigned mn_ = (x) > (y) ? (y) : (x); (x) = mx_; (y) = mn_; } while (0)
; DI void merge16_desc(unsigned (&a)[16], const unsigned (&b)[16]) {
; #pragma unroll
;   for (int i = 0; i < 16; ++i) a[i] = a[i] > b[15 - i] ? a[i] : b[15 - i];
; #pragma unroll
;   for (int j = 8; j > 0; j >>= 1)
; #pragma unroll
;     for (int i = 0; i < 16; ++i) if ((i & j) == 0) CE_DESC(a[i], a[i + j]);
; }
; template <int CTRL> DI void dpp16(unsigned (&b)[16], const unsigned (&a)[16]) {
; #pragma unroll
;   for (int s = 0; s < 16; ++s) b[s] = (unsigned)__builtin_amdgcn_update_dpp(0, (int)a[s], CTRL, 0xF, 0xF, true);
; }
; DI void peer_select_unit(const Params& p, int unit, char* lds, const bf16x8 (&kb)[4][4]) {
;     ...
;     dpp16<0xB1>(bq, a); merge16_desc(a, bq);
;     dpp16<0x4E>(bq, a); merge16_desc(a, bq);
;     dpp16<0x141>(bq, a); merge16_desc(a, bq);
; #pragma unroll
;     for (int s = 0; s < 2; ++s) {
;       unsigned k = 0u;
; #pragma unroll
;       for (int q = 0; q < 8; ++q) k = part == q ? a[2 * q + s] : k;
	v_max_u32_e32 v217, v222, v196
	v_max_u32_e32 v231, v235, v195
	v_max_u32_e32 v144, v145, v194
	v_max_u32_e32 v137, v219, v213
	v_min_u32_e32 v228, v219, v213
	v_max_u32_e32 v124, v216, v229
	v_min_u32_e32 v138, v216, v229
	v_max_u32_e32 v225, v223, v221
	v_min_u32_e32 v230, v223, v221
	v_max_u32_e32 v139, v220, v122
	v_min_u32_e32 v136, v220, v122
	v_max_u32_e32 v130, v234, v214
	v_min_u32_e32 v233, v234, v214
	v_max_u32_e32 v232, v126, v217
	v_min_u32_e32 v127, v126, v217
	v_max_u32_e32 v134, v215, v231
	v_min_u32_e32 v212, v215, v231
	v_max_u32_e32 v123, v129, v144
	v_min_u32_e32 v227, v129, v144
	v_max_u32_e32 v131, v137, v130
	v_min_u32_e32 v125, v137, v130
	v_max_u32_e32 v135, v124, v232
	v_min_u32_e32 v133, v124, v232
	v_max_u32_e32 v128, v225, v134
	v_min_u32_e32 v226, v225, v134
	v_max_u32_e32 v132, v139, v123
	v_min_u32_e32 v224, v139, v123
	v_max_u32_e32 v218, v228, v233
	v_min_u32_e32 v222, v228, v233
	v_max_u32_e32 v235, v138, v127
	v_min_u32_e32 v145, v138, v127
	v_max_u32_e32 v194, v230, v212
	v_min_u32_e32 v195, v230, v212
	v_max_u32_e32 v196, v136, v227
	v_min_u32_e32 v197, v136, v227
	v_max_u32_e32 v198, v131, v128
	v_min_u32_e32 v199, v131, v128
	v_max_u32_e32 v200, v135, v132
	v_min_u32_e32 v201, v135, v132
	v_max_u32_e32 v202, v125, v226
	v_min_u32_e32 v203, v125, v226
	v_max_u32_e32 v204, v133, v224
	v_min_u32_e32 v205, v133, v224
	v_max_u32_e32 v140, v218, v194
	v_min_u32_e32 v141, v218, v194
	v_max_u32_e32 v142, v235, v196
	v_min_u32_e32 v143, v235, v196
	v_max_u32_e32 v219, v222, v195
	v_min_u32_e32 v213, v222, v195
	v_max_u32_e32 v216, v145, v197
	v_min_u32_e32 v229, v145, v197
	v_max_u32_e32 v223, v198, v200
	v_min_u32_e32 v221, v198, v200
	v_max_u32_e32 v220, v199, v201
	v_min_u32_e32 v122, v199, v201
	v_max_u32_e32 v234, v202, v204
	v_min_u32_e32 v214, v202, v204
	v_max_u32_e32 v126, v203, v205
	v_min_u32_e32 v217, v203, v205
	v_max_u32_e32 v215, v140, v142
	v_min_u32_e32 v231, v140, v142
	v_max_u32_e32 v129, v141, v143
	v_min_u32_e32 v144, v141, v143
	v_max_u32_e32 v137, v219, v216
	v_min_u32_e32 v130, v219, v216
	v_max_u32_e32 v124, v213, v229
	v_min_u32_e32 v232, v213, v229
	s_nop 1
	v_max_u32_dpp v225, v232, v223 quad_perm:[1,0,3,2] row_mask:0xf bank_mask:0xf
	v_max_u32_dpp v134, v124, v221 quad_perm:[1,0,3,2] row_mask:0xf bank_mask:0xf
	v_max_u32_dpp v139, v130, v220 quad_perm:[1,0,3,2] row_mask:0xf bank_mask:0xf
	v_max_u32_dpp v123, v137, v122 quad_perm:[1,0,3,2] row_mask:0xf bank_mask:0xf
	v_max_u32_dpp v228, v144, v234 quad_perm:[1,0,3,2] row_mask:0xf bank_mask:0xf
	v_max_u32_dpp v233, v129, v214 quad_perm:[1,0,3,2] row_mask:0xf bank_mask:0xf
	v_max_u32_dpp v138, v231, v126 quad_perm:[1,0,3,2] row_mask:0xf bank_mask:0xf
	v_max_u32_dpp v127, v215, v217 quad_perm:[1,0,3,2] row_mask:0xf bank_mask:0xf
	v_max_u32_dpp v230, v217, v215 quad_perm:[1,0,3,2] row_mask:0xf bank_mask:0xf
	v_max_u32_dpp v212, v126, v231 quad_perm:[1,0,3,2] row_mask:0xf bank_mask:0xf
	v_max_u32_dpp v136, v214, v129 quad_perm:[1,0,3,2] row_mask:0xf bank_mask:0xf
	v_max_u32_dpp v227, v234, v144 quad_perm:[1,0,3,2] row_mask:0xf bank_mask:0xf
	v_max_u32_dpp v131, v122, v137 quad_perm:[1,0,3,2] row_mask:0xf bank_mask:0xf
	v_max_u32_dpp v128, v220, v130 quad_perm:[1,0,3,2] row_mask:0xf bank_mask:0xf
	v_max_u32_dpp v135, v221, v124 quad_perm:[1,0,3,2] row_mask:0xf bank_mask:0xf
	v_max_u32_dpp v132, v223, v232 quad_perm:[1,0,3,2] row_mask:0xf bank_mask:0xf
	v_max_u32_e32 v125, v225, v230
	v_min_u32_e32 v226, v225, v230
	v_max_u32_e32 v133, v134, v212
	v_min_u32_e32 v224, v134, v212
	v_max_u32_e32 v218, v139, v136
	v_min_u32_e32 v194, v139, v136
	v_max_u32_e32 v235, v123, v227
	v_min_u32_e32 v196, v123, v227
	v_max_u32_e32 v222, v228, v131
	v_min_u32_e32 v195, v228, v131
	v_max_u32_e32 v145, v233, v128
	v_min_u32_e32 v197, v233, v128
	v_max_u32_e32 v198, v138, v135
	v_min_u32_e32 v200, v138, v135
	v_max_u32_e32 v199, v127, v132
	v_min_u32_e32 v201, v127, v132
	v_max_u32_e32 v202, v125, v222
	v_min_u32_e32 v204, v125, v222
	v_max_u32_e32 v203, v133, v145
	v_min_u32_e32 v205, v133, v145
	v_max_u32_e32 v140, v218, v198
	v_min_u32_e32 v142, v218, v198
	v_max_u32_e32 v141, v235, v199
	v_min_u32_e32 v143, v235, v199
	v_max_u32_e32 v219, v226, v195
	v_min_u32_e32 v216, v226, v195
	v_max_u32_e32 v213, v224, v197
	v_min_u32_e32 v229, v224, v197
	v_max_u32_e32 v223, v194, v200
	v_min_u32_e32 v221, v194, v200
	v_max_u32_e32 v220, v196, v201
	v_min_u32_e32 v122, v196, v201
	v_max_u32_e32 v234, v202, v140
	v_min_u32_e32 v214, v202, v140
	v_max_u32_e32 v126, v203, v141
	v_min_u32_e32 v217, v203, v141
	v_max_u32_e32 v215, v204, v142
	v_min_u32_e32 v231, v204, v142
	v_max_u32_e32 v129, v205, v143
	v_min_u32_e32 v144, v205, v143
	v_max_u32_e32 v137, v219, v223
	v_min_u32_e32 v130, v219, v223
	v_max_u32_e32 v124, v213, v220
	v_min_u32_e32 v232, v213, v220
	v_max_u32_e32 v225, v216, v221
	v_min_u32_e32 v230, v216, v221
	v_max_u32_e32 v134, v229, v122
	v_min_u32_e32 v212, v229, v122
	v_max_u32_e32 v139, v234, v126
	v_min_u32_e32 v136, v234, v126
	v_max_u32_e32 v123, v214, v217
	v_min_u32_e32 v227, v214, v217
	v_max_u32_e32 v228, v215, v129
	v_min_u32_e32 v131, v215, v129
	v_max_u32_e32 v233, v231, v144
	v_min_u32_e32 v128, v231, v144
	v_max_u32_e32 v138, v137, v124
	v_min_u32_e32 v135, v137, v124
	v_max_u32_e32 v127, v130, v232
	v_min_u32_e32 v132, v130, v232
	v_max_u32_e32 v125, v225, v134
	v_min_u32_e32 v222, v225, v134
	v_max_u32_e32 v133, v230, v212
	v_min_u32_e32 v145, v230, v212
	v_mov_b32_e32 v198, v227
	v_mov_b32_e32 v235, v222
	v_cmp_eq_u32_e32 vcc, 1, v237
	s_nop 1
	v_cndmask_b32_e32 v199, v139, v138, vcc
	v_cndmask_b32_e32 v195, v136, v135, vcc
; DI void peer_select_unit(const Params& p, int unit, char* lds, const bf16x8 (&kb)[4][4]) {
;     ...
; #pragma unroll
;     for (int s = 0; s < 2; ++s) {
;       unsigned k = 0u;
; #pragma unroll
;       for (int q = 0; q < 8; ++q) k = part == q ? a[2 * q + s] : k;
;       const int idx = 127 - (int)(k & 127u);
;       topv[rr * 16 + 2 * part + s] = sc[rr * 132 + idx]; topi[rr * 16 + 2 * part + s] = idx;
;     }
;   }
;   __syncthreads();
;   if (tid < 128) {
;     const int tok = tid >> 2, q4 = tid & 3;
;     unsigned c[16], bq[16];
; #pragma unroll
;     for (int i = 0; i < 16; ++i) {
;       const unsigned code = PEER_CAND[16 * q4 + i];
;       const float v = topv[tok * 16 + ((code >> 4) & 15)] + topv[(32 + tok) * 16 + (code & 15)];
	v_cndmask_b32_e32 v197, v123, v127, vcc
	v_cndmask_b32_e32 v194, v198, v132, vcc
	v_cndmask_b32_e32 v200, v228, v125, vcc
	v_cndmask_b32_e32 v196, v131, v235, vcc
	v_cndmask_b32_e32 v201, v233, v133, vcc
	v_cndmask_b32_e32 v202, v128, v145, vcc
	v_and_b32_e32 v240, 0x7f, v199
	v_sub_u32_e32 v212, 0x7f, v240
	v_lshl_add_u32 v199, v212, 2, v238
	ds_read_b32 v220, v199
	v_and_b32_e32 v240, 0x7f, v195
	v_sub_u32_e32 v213, 0x7f, v240
	v_lshl_add_u32 v195, v213, 2, v238
	ds_read_b32 v221, v195
	v_and_b32_e32 v240, 0x7f, v197
	v_sub_u32_e32 v214, 0x7f, v240
	v_lshl_add_u32 v197, v214, 2, v238
	ds_read_b32 v222, v197
	v_and_b32_e32 v240, 0x7f, v194
	v_sub_u32_e32 v215, 0x7f, v240
	v_lshl_add_u32 v194, v215, 2, v238
	ds_read_b32 v223, v194
	v_and_b32_e32 v240, 0x7f, v200
	v_sub_u32_e32 v216, 0x7f, v240
	v_lshl_add_u32 v200, v216, 2, v238
	ds_read_b32 v224, v200
	v_and_b32_e32 v240, 0x7f, v196
	v_sub_u32_e32 v217, 0x7f, v240
	v_lshl_add_u32 v196, v217, 2, v238
	ds_read_b32 v225, v196
	v_and_b32_e32 v240, 0x7f, v201
	v_sub_u32_e32 v218, 0x7f, v240
	v_lshl_add_u32 v201, v218, 2, v238
	ds_read_b32 v226, v201
	v_and_b32_e32 v240, 0x7f, v202
	v_sub_u32_e32 v219, 0x7f, v240
	v_lshl_add_u32 v202, v219, 2, v238
	ds_read_b32 v227, v202
	v_lshlrev_b32_e32 v239, 6, v236
	v_lshl_add_u32 v239, v237, 5, v239
	v_add_u32_e32 v239, v146, v239
	ds_write_b128 v239, v[212:215] offset:37888
	ds_write_b128 v239, v[216:219] offset:37904
	s_waitcnt lgkmcnt(2)
	ds_write_b128 v239, v[220:223] offset:33792
	ds_write_b128 v239, v[224:227] offset:33808
.Lps2b_skip:
	s_or_b64 exec, exec, s[8:9]
	v_xor_b32_e32 v66, v249, v66
	v_cmp_gt_i32_e32 vcc, s18, v66
	s_waitcnt lgkmcnt(0)
	s_barrier
	s_and_saveexec_b64 s[8:9], vcc
	s_cbranch_execz .LBB0_1651
	v_and_b32_e32 v77, 3, v66
	v_lshrrev_b32_e32 v75, 2, v66
	v_lshlrev_b32_e32 v64, 4, v77
	v_and_b32_e32 v80, 0xffff, v244
	v_lshlrev_b32_e32 v66, 6, v75
	v_lshlrev_b32_e32 v76, 4, v75
	v_cmp_eq_u32_e32 vcc, 3, v77
	v_cmp_ne_u32_e64 s[0:1], 3, v77
	v_mov_b32_e32 v82, 0
	v_lshrrev_b32_e32 v67, 2, v80
	v_and_b32_e32 v68, 15, v80
	v_lshrrev_b16_e32 v79, 8, v80
	v_and_b32_e32 v67, 60, v67
	v_lshlrev_b32_e32 v68, 2, v68
	v_lshrrev_b32_e32 v69, 2, v79
	v_and_b32_e32 v78, 15, v79
	v_add3_u32 v67, v146, v67, v66
	v_add3_u32 v68, v146, v68, v66
	v_and_b32_e32 v69, 60, v69
	v_lshlrev_b32_e32 v78, 2, v78
	v_add3_u32 v81, v146, v69, v66
	v_add3_u32 v78, v146, v78, v66
	ds_read_b32 v67, v67 offset:33792
	ds_read_b32 v69, v68 offset:35840
	ds_read_b32 v66, v81 offset:33792
	ds_read_b32 v68, v78 offset:35840
	v_mov_b32_e32 v81, 0
	v_lshlrev_b32_e32 v78, 2, v76
	v_mov_b32_e32 v83, 0
	v_mov_b32_e32 v84, 0
	v_mov_b32_e32 v85, 0
	v_mov_b32_e32 v86, 0
	v_mov_b32_e32 v87, 0
	v_mov_b32_e32 v88, 0
	v_mov_b32_e32 v89, 0
	v_mov_b32_e32 v90, 0
	v_mov_b32_e32 v91, 0
	v_mov_b32_e32 v92, 0
	v_mov_b32_e32 v93, 0
	v_mov_b32_e32 v94, 0
	s_and_saveexec_b64 s[6:7], s[0:1]
	v_bfe_u32 v82, v244, 16, 8
	v_lshrrev_b32_e32 v238, 2, v82
	v_and_b32_e32 v239, 15, v82
	v_and_b32_e32 v238, 60, v238
	v_lshlrev_b32_e32 v239, 2, v239
	v_add3_u32 v238, v146, v238, v78
	v_add3_u32 v239, v146, v239, v78
	ds_read_b32 v210, v238 offset:33792
	ds_read_b32 v211, v239 offset:35840
	v_bfe_u32 v81, v244, 24, 8
	v_lshrrev_b32_e32 v238, 2, v81
	v_and_b32_e32 v239, 15, v81
	v_and_b32_e32 v238, 60, v238
	v_lshlrev_b32_e32 v239, 2, v239
	v_add3_u32 v238, v146, v238, v78
	v_add3_u32 v239, v146, v239, v78
	ds_read_b32 v212, v238 offset:33792
	ds_read_b32 v213, v239 offset:35840
	v_bfe_u32 v84, v245, 0, 8
	v_lshrrev_b32_e32 v238, 2, v84
	v_and_b32_e32 v239, 15, v84
	v_and_b32_e32 v238, 60, v238
	v_lshlrev_b32_e32 v239, 2, v239
	v_add3_u32 v238, v146, v238, v78
	v_add3_u32 v239, v146, v239, v78
	ds_read_b32 v214, v238 offset:33792
	ds_read_b32 v215, v239 offset:35840
	v_bfe_u32 v83, v245, 8, 8
	v_lshrrev_b32_e32 v238, 2, v83
	v_and_b32_e32 v239, 15, v83
	v_and_b32_e32 v238, 60, v238
	v_lshlrev_b32_e32 v239, 2, v239
	v_add3_u32 v238, v146, v238, v78
	v_add3_u32 v239, v146, v239, v78
	ds_read_b32 v216, v238 offset:33792
	ds_read_b32 v217, v239 offset:35840
	v_bfe_u32 v86, v245, 16, 8
	v_lshrrev_b32_e32 v238, 2, v86
	v_and_b32_e32 v239, 15, v86
	v_and_b32_e32 v238, 60, v238
	v_lshlrev_b32_e32 v239, 2, v239
	v_add3_u32 v238, v146, v238, v78
	v_add3_u32 v239, v146, v239, v78
	ds_read_b32 v218, v238 offset:33792
	ds_read_b32 v219, v239 offset:35840
	v_bfe_u32 v85, v245, 24, 8
	v_lshrrev_b32_e32 v238, 2, v85
	v_and_b32_e32 v239, 15, v85
	v_and_b32_e32 v238, 60, v238
	v_lshlrev_b32_e32 v239, 2, v239
	v_add3_u32 v238, v146, v238, v78
	v_add3_u32 v239, v146, v239, v78
	ds_read_b32 v220, v238 offset:33792
	ds_read_b32 v221, v239 offset:35840
	v_bfe_u32 v88, v246, 0, 8
	v_lshrrev_b32_e32 v238, 2, v88
	v_and_b32_e32 v239, 15, v88
	v_and_b32_e32 v238, 60, v238
	v_lshlrev_b32_e32 v239, 2, v239
	v_add3_u32 v238, v146, v238, v78
	v_add3_u32 v239, v146, v239, v78
	ds_read_b32 v222, v238 offset:33792
	ds_read_b32 v223, v239 offset:35840
	v_bfe_u32 v87, v246, 8, 8
	v_lshrrev_b32_e32 v238, 2, v87
	v_and_b32_e32 v239, 15, v87
	v_and_b32_e32 v238, 60, v238
	v_lshlrev_b32_e32 v239, 2, v239
	v_add3_u32 v238, v146, v238, v78
	v_add3_u32 v239, v146, v239, v78
	ds_read_b32 v224, v238 offset:33792
	ds_read_b32 v225, v239 offset:35840
	v_bfe_u32 v90, v246, 16, 8
	v_lshrrev_b32_e32 v238, 2, v90
	v_and_b32_e32 v239, 15, v90
	v_and_b32_e32 v238, 60, v238
	v_lshlrev_b32_e32 v239, 2, v239
	v_add3_u32 v238, v146, v238, v78
	v_add3_u32 v239, v146, v239, v78
	ds_read_b32 v226, v238 offset:33792
	ds_read_b32 v227, v239 offset:35840
	v_bfe_u32 v89, v246, 24, 8
	v_lshrrev_b32_e32 v238, 2, v89
	v_and_b32_e32 v239, 15, v89
	v_and_b32_e32 v238, 60, v238
	v_lshlrev_b32_e32 v239, 2, v239
	v_add3_u32 v238, v146, v238, v78
	v_add3_u32 v239, v146, v239, v78
	ds_read_b32 v228, v238 offset:33792
	ds_read_b32 v229, v239 offset:35840
	v_bfe_u32 v92, v247, 0, 8
	v_lshrrev_b32_e32 v238, 2, v92
	v_and_b32_e32 v239, 15, v92
	v_and_b32_e32 v238, 60, v238
	v_lshlrev_b32_e32 v239, 2, v239
	v_add3_u32 v238, v146, v238, v78
	v_add3_u32 v239, v146, v239, v78
	ds_read_b32 v230, v238 offset:33792
	ds_read_b32 v231, v239 offset:35840
	v_bfe_u32 v91, v247, 8, 8
	v_lshrrev_b32_e32 v238, 2, v91
	v_and_b32_e32 v239, 15, v91
	v_and_b32_e32 v238, 60, v238
	v_lshlrev_b32_e32 v239, 2, v239
	v_add3_u32 v238, v146, v238, v78
	v_add3_u32 v239, v146, v239, v78
	ds_read_b32 v232, v238 offset:33792
	ds_read_b32 v233, v239 offset:35840
	v_bfe_u32 v94, v247, 16, 8
	v_lshrrev_b32_e32 v238, 2, v94
	v_and_b32_e32 v239, 15, v94
	v_and_b32_e32 v238, 60, v238
	v_lshlrev_b32_e32 v239, 2, v239
	v_add3_u32 v238, v146, v238, v78
	v_add3_u32 v239, v146, v239, v78
	ds_read_b32 v234, v238 offset:33792
	ds_read_b32 v235, v239 offset:35840
	v_bfe_u32 v70, v247, 24, 8
	v_lshrrev_b32_e32 v238, 2, v70
	v_and_b32_e32 v239, 15, v70
	v_and_b32_e32 v238, 60, v238
	v_lshlrev_b32_e32 v239, 2, v239
	v_add3_u32 v238, v146, v238, v78
	v_add3_u32 v239, v146, v239, v78
	ds_read_b32 v236, v238 offset:33792
	ds_read_b32 v237, v239 offset:35840
	s_waitcnt lgkmcnt(0)
; DI unsigned ordkey(float f) { const unsigned u = __float_as_uint(f); return (u & 0x80000000u) ? ~u : (u | 0x80000000u); }
; DI void peer_select_unit(const Params& p, int unit, char* lds, const bf16x8 (&kb)[4][4]) {
;     ...
; #pragma unroll
;     for (int i = 0; i < 16; ++i) {
;       const unsigned code = PEER_CAND[16 * q4 + i];
;       const float v = topv[tok * 16 + ((code >> 4) & 15)] + topv[(32 + tok) * 16 + (code & 15)];
;       c[i] = code == 0xFFu ? 0u : ((ordkey(v) & ~255u) | (255u - code));
;     }
	v_add_f32_e32 v210, v210, v211
	v_cmp_gt_i32_e64 s[4:5], 0, v210
	v_not_b32_e32 v211, v210
	v_or_b32_e32 v238, 0x80000000, v210
	v_cndmask_b32_e64 v210, v238, v211, s[4:5]
	v_and_b32_e32 v210, 0xffffff00, v210
	v_bitop3_b32 v82, v210, s19, v82 bitop3:0x36
	v_add_f32_e32 v212, v212, v213
	v_cmp_gt_i32_e64 s[4:5], 0, v212
	v_not_b32_e32 v213, v212
	v_or_b32_e32 v238, 0x80000000, v212
	v_cndmask_b32_e64 v212, v238, v213, s[4:5]
	v_and_b32_e32 v212, 0xffffff00, v212
	v_bitop3_b32 v81, v212, s19, v81 bitop3:0x36
	v_add_f32_e32 v214, v214, v215
	v_cmp_gt_i32_e64 s[4:5], 0, v214
	v_not_b32_e32 v215, v214
	v_or_b32_e32 v238, 0x80000000, v214
	v_cndmask_b32_e64 v214, v238, v215, s[4:5]
	v_and_b32_e32 v214, 0xffffff00, v214
	v_bitop3_b32 v84, v214, s19, v84 bitop3:0x36
	v_add_f32_e32 v216, v216, v217
	v_cmp_gt_i32_e64 s[4:5], 0, v216
	v_not_b32_e32 v217, v216
	v_or_b32_e32 v238, 0x80000000, v216
	v_cndmask_b32_e64 v216, v238, v217, s[4:5]
	v_and_b32_e32 v216, 0xffffff00, v216
	v_bitop3_b32 v83, v216, s19, v83 bitop3:0x36
	v_add_f32_e32 v218, v218, v219
	v_cmp_gt_i32_e64 s[4:5], 0, v218
	v_not_b32_e32 v219, v218
	v_or_b32_e32 v238, 0x80000000, v218
	v_cndmask_b32_e64 v218, v238, v219, s[4:5]
	v_and_b32_e32 v218, 0xffffff00, v218
	v_bitop3_b32 v86, v218, s19, v86 bitop3:0x36
	v_add_f32_e32 v220, v220, v221
	v_cmp_gt_i32_e64 s[4:5], 0, v220
	v_not_b32_e32 v221, v220
	v_or_b32_e32 v238, 0x80000000, v220
	v_cndmask_b32_e64 v220, v238, v221, s[4:5]
	v_and_b32_e32 v220, 0xffffff00, v220
	v_bitop3_b32 v85, v220, s19, v85 bitop3:0x36
	v_add_f32_e32 v222, v222, v223
	v_cmp_gt_i32_e64 s[4:5], 0, v222
	v_not_b32_e32 v223, v222
	v_or_b32_e32 v238, 0x80000000, v222
	v_cndmask_b32_e64 v222, v238, v223, s[4:5]
	v_and_b32_e32 v222, 0xffffff00, v222
	v_bitop3_b32 v88, v222, s19, v88 bitop3:0x36
	v_add_f32_e32 v224, v224, v225
	v_cmp_gt_i32_e64 s[4:5], 0, v224
	v_not_b32_e32 v225, v224
	v_or_b32_e32 v238, 0x80000000, v224
	v_cndmask_b32_e64 v224, v238, v225, s[4:5]
	v_and_b32_e32 v224, 0xffffff00, v224
	v_bitop3_b32 v87, v224, s19, v87 bitop3:0x36
	v_add_f32_e32 v226, v226, v227
	v_cmp_gt_i32_e64 s[4:5], 0, v226
	v_not_b32_e32 v227, v226
	v_or_b32_e32 v238, 0x80000000, v226
	v_cndmask_b32_e64 v226, v238, v227, s[4:5]
	v_and_b32_e32 v226, 0xffffff00, v226
	v_bitop3_b32 v90, v226, s19, v90 bitop3:0x36
	v_add_f32_e32 v228, v228, v229
	v_cmp_gt_i32_e64 s[4:5], 0, v228
	v_not_b32_e32 v229, v228
	v_or_b32_e32 v238, 0x80000000, v228
	v_cndmask_b32_e64 v228, v238, v229, s[4:5]
	v_and_b32_e32 v228, 0xffffff00, v228
	v_bitop3_b32 v89, v228, s19, v89 bitop3:0x36
	v_add_f32_e32 v230, v230, v231
	v_cmp_gt_i32_e64 s[4:5], 0, v230
	v_not_b32_e32 v231, v230
	v_or_b32_e32 v238, 0x80000000, v230
	v_cndmask_b32_e64 v230, v238, v231, s[4:5]
	v_and_b32_e32 v230, 0xffffff00, v230
	v_bitop3_b32 v92, v230, s19, v92 bitop3:0x36
	v_add_f32_e32 v232, v232, v233
	v_cmp_gt_i32_e64 s[4:5], 0, v232
	v_not_b32_e32 v233, v232
	v_or_b32_e32 v238, 0x80000000, v232
	v_cndmask_b32_e64 v232, v238, v233, s[4:5]
	v_and_b32_e32 v232, 0xffffff00, v232
	v_bitop3_b32 v91, v232, s19, v91 bitop3:0x36
	v_add_f32_e32 v234, v234, v235
	v_cmp_gt_i32_e64 s[4:5], 0, v234
	v_not_b32_e32 v235, v234
	v_or_b32_e32 v238, 0x80000000, v234
	v_cndmask_b32_e64 v234, v238, v235, s[4:5]
	v_and_b32_e32 v234, 0xffffff00, v234
	v_bitop3_b32 v94, v234, s19, v94 bitop3:0x36
	v_add_f32_e32 v236, v236, v237
	v_cmp_gt_i32_e64 s[4:5], 0, v236
	v_not_b32_e32 v237, v236
	v_or_b32_e32 v238, 0x80000000, v236
	v_cndmask_b32_e64 v236, v238, v237, s[4:5]
	v_and_b32_e32 v236, 0xffffff00, v236
	v_bitop3_b32 v93, v236, s19, v70 bitop3:0x36
	s_or_b64 exec, exec, s[6:7]
	s_mov_b64 s[4:5], exec
	s_branch .LBB0_1650
